# adds gMLP unit epilogue: g_v / b_s loaded once together (was 32 dependent dword round trips), the 4 u-row loads issued together
# speedup vs baseline: 1.0174x; 1.0016x over previous
.LBB0_1215:
	s_add_u32 s8, s8, s6
	v_lshl_or_b32 v1, v47, 2, s2
	s_addc_u32 s9, s9, s7
	v_add_u32_e32 v4, s72, v1
	s_add_u32 s0, s10, s6
	v_or_b32_e32 v2, s72, v46
	v_ashrrev_i32_e32 v5, 31, v4
	s_movk_i32 s3, 0x110
	s_addc_u32 s1, s11, s7
	v_lshlrev_b32_e32 v40, 1, v46
	v_lshlrev_b32_e32 v2, 2, v2
	v_lshl_add_u64 v[4:5], v[4:5], 2, s[8:9]
	v_mul_lo_u32 v1, v1, s3
	global_load_dwordx4 v[42:45], v[4:5], off
	v_add3_u32 v1, 0, v40, v1
	global_load_dword v50, v2, s[0:1]
	global_load_dword v51, v2, s[0:1] offset:64
	global_load_dword v52, v2, s[0:1] offset:128
	global_load_dword v53, v2, s[0:1] offset:192
	global_load_dword v54, v2, s[0:1] offset:256
	global_load_dword v55, v2, s[0:1] offset:320
	global_load_dword v56, v2, s[0:1] offset:384
	global_load_dword v57, v2, s[0:1] offset:448
	s_lshl_b32 s2, s72, 1
	s_waitcnt vmcnt(0)
	v_fma_f32 v36, v36, v50, v42
	v_cvt_pk_bf16_f32 v36, v36, v3
	ds_write_b16 v1, v36 offset:36864
	v_fma_f32 v32, v32, v51, v42
	v_cvt_pk_bf16_f32 v32, v32, v3
	ds_write_b16 v1, v32 offset:36896
	v_fma_f32 v28, v28, v52, v42
	v_cvt_pk_bf16_f32 v28, v28, v3
	ds_write_b16 v1, v28 offset:36928
	v_fma_f32 v24, v24, v53, v42
	v_cvt_pk_bf16_f32 v24, v24, v3
	ds_write_b16 v1, v24 offset:36960
	v_fma_f32 v20, v20, v54, v42
	v_cvt_pk_bf16_f32 v20, v20, v3
	ds_write_b16 v1, v20 offset:36992
	v_fma_f32 v14, v14, v55, v42
	v_cvt_pk_bf16_f32 v14, v14, v3
	ds_write_b16 v1, v14 offset:37024
	v_fma_f32 v10, v10, v56, v42
	v_cvt_pk_bf16_f32 v10, v10, v3
	ds_write_b16 v1, v10 offset:37056
	v_fma_f32 v6, v6, v57, v42
	v_cvt_pk_bf16_f32 v6, v6, v3
	ds_write_b16 v1, v6 offset:37088
	v_fma_f32 v37, v37, v50, v43
	v_cvt_pk_bf16_f32 v37, v37, v3
	ds_write_b16 v1, v37 offset:37136
	v_fma_f32 v33, v33, v51, v43
	v_cvt_pk_bf16_f32 v33, v33, v3
	ds_write_b16 v1, v33 offset:37168
	v_fma_f32 v29, v29, v52, v43
	v_cvt_pk_bf16_f32 v29, v29, v3
	ds_write_b16 v1, v29 offset:37200
	v_fma_f32 v25, v25, v53, v43
	v_cvt_pk_bf16_f32 v25, v25, v3
	ds_write_b16 v1, v25 offset:37232
	v_fma_f32 v21, v21, v54, v43
	v_cvt_pk_bf16_f32 v21, v21, v3
	ds_write_b16 v1, v21 offset:37264
	v_fma_f32 v15, v15, v55, v43
	v_cvt_pk_bf16_f32 v15, v15, v3
	ds_write_b16 v1, v15 offset:37296
	v_fma_f32 v11, v11, v56, v43
	v_cvt_pk_bf16_f32 v11, v11, v3
	ds_write_b16 v1, v11 offset:37328
	v_fma_f32 v7, v7, v57, v43
	v_cvt_pk_bf16_f32 v7, v7, v3
	ds_write_b16 v1, v7 offset:37360
	v_fma_f32 v38, v38, v50, v44
	v_cvt_pk_bf16_f32 v38, v38, v3
	ds_write_b16 v1, v38 offset:37408
	v_fma_f32 v34, v34, v51, v44
	v_cvt_pk_bf16_f32 v34, v34, v3
	ds_write_b16 v1, v34 offset:37440
	v_fma_f32 v30, v30, v52, v44
	v_cvt_pk_bf16_f32 v30, v30, v3
	ds_write_b16 v1, v30 offset:37472
	v_fma_f32 v26, v26, v53, v44
	v_cvt_pk_bf16_f32 v26, v26, v3
	ds_write_b16 v1, v26 offset:37504
	v_fma_f32 v22, v22, v54, v44
	v_cvt_pk_bf16_f32 v22, v22, v3
	ds_write_b16 v1, v22 offset:37536
	v_fma_f32 v16, v16, v55, v44
	v_cvt_pk_bf16_f32 v16, v16, v3
	ds_write_b16 v1, v16 offset:37568
	v_fma_f32 v12, v12, v56, v44
	v_cvt_pk_bf16_f32 v12, v12, v3
	ds_write_b16 v1, v12 offset:37600
	v_fma_f32 v8, v8, v57, v44
	v_cvt_pk_bf16_f32 v8, v8, v3
	ds_write_b16 v1, v8 offset:37632
	v_fma_f32 v39, v39, v50, v45
	v_cvt_pk_bf16_f32 v39, v39, v3
	ds_write_b16 v1, v39 offset:37680
	v_fma_f32 v35, v35, v51, v45
	v_cvt_pk_bf16_f32 v35, v35, v3
	ds_write_b16 v1, v35 offset:37712
	v_fma_f32 v31, v31, v52, v45
	v_cvt_pk_bf16_f32 v31, v31, v3
	ds_write_b16 v1, v31 offset:37744
	v_fma_f32 v27, v27, v53, v45
	v_cvt_pk_bf16_f32 v27, v27, v3
	ds_write_b16 v1, v27 offset:37776
	v_fma_f32 v23, v23, v54, v45
	v_cvt_pk_bf16_f32 v23, v23, v3
	ds_write_b16 v1, v23 offset:37808
	v_fma_f32 v17, v17, v55, v45
	v_cvt_pk_bf16_f32 v17, v17, v3
	ds_write_b16 v1, v17 offset:37840
	v_fma_f32 v13, v13, v56, v45
	v_cvt_pk_bf16_f32 v13, v13, v3
	ds_write_b16 v1, v13 offset:37872
	v_fma_f32 v9, v9, v57, v45
	v_cvt_pk_bf16_f32 v9, v9, v3
	ds_write_b16 v1, v9 offset:37904
	s_add_u32 s0, s28, s2
	s_addc_u32 s1, s29, 0
	v_lshlrev_b32_e32 v1, 4, v19
	v_and_b32_e32 v2, 0xf0, v1
	v_lshl_add_u64 v[6:7], s[0:1], 0, v[2:3]
	s_add_u32 s0, s14, s2
	v_ashrrev_i32_e32 v1, 4, v19
	s_addc_u32 s1, s15, 0
	v_add_u32_e32 v20, s21, v1
	v_lshl_add_u64 v[4:5], s[0:1], 0, v[2:3]
	v_mad_i64_i32 v[14:15], s[0:1], v20, s96, v[6:7]
	s_waitcnt lgkmcnt(0)
	s_barrier
	s_mov_b64 vcc, 0x28000
	v_lshl_add_u64 v[36:37], v[14:15], 0, vcc
	v_lshl_add_u64 v[38:39], v[36:37], 0, vcc
	v_lshl_add_u64 v[22:23], v[38:39], 0, vcc
	global_load_dwordx4 v[14:17], v[14:15], off
	global_load_dwordx4 v[24:27], v[36:37], off
	global_load_dwordx4 v[28:31], v[38:39], off
	global_load_dwordx4 v[32:35], v[22:23], off
	v_add_u32_e32 v8, 0, v2
	v_mad_u64_u32 v[10:11], s[0:1], v1, s3, v[8:9]
	ds_read_b128 v[10:13], v10 offset:36864
	v_ashrrev_i32_e32 v21, 31, v20
	s_add_i32 s20, s20, s22
	s_add_i32 s16, s16, s17
	s_add_i32 s18, s18, s19
	s_waitcnt lgkmcnt(0)
	v_lshlrev_b32_e32 v1, 16, v10
	v_and_b32_e32 v9, 0xffff0000, v10
	s_cmpk_gt_i32 s20, 0x1ff
	s_waitcnt vmcnt(3)
	v_lshlrev_b32_e32 v2, 16, v14
	v_mul_f32_e32 v1, v2, v1
	v_and_b32_e32 v2, 0xffff0000, v14
	v_mul_f32_e32 v2, v2, v9
	v_cvt_pk_bf16_f32 v10, v1, v2
	v_lshlrev_b32_e32 v1, 16, v11
	v_lshlrev_b32_e32 v2, 16, v15
	v_mul_f32_e32 v1, v2, v1
	v_and_b32_e32 v2, 0xffff0000, v15
	v_and_b32_e32 v9, 0xffff0000, v11
	v_mul_f32_e32 v2, v2, v9
	v_cvt_pk_bf16_f32 v11, v1, v2
	v_lshlrev_b32_e32 v1, 16, v12
	v_lshlrev_b32_e32 v2, 16, v16
	v_mul_f32_e32 v1, v2, v1
	v_and_b32_e32 v2, 0xffff0000, v16
	v_and_b32_e32 v9, 0xffff0000, v12
	v_mul_f32_e32 v2, v2, v9
	v_cvt_pk_bf16_f32 v12, v1, v2
	v_lshlrev_b32_e32 v1, 16, v13
	v_lshlrev_b32_e32 v2, 16, v17
	v_mul_f32_e32 v1, v2, v1
	v_and_b32_e32 v2, 0xffff0000, v17
	v_and_b32_e32 v9, 0xffff0000, v13
	v_mul_f32_e32 v2, v2, v9
	v_cvt_pk_bf16_f32 v13, v1, v2
	v_add_u32_e32 v1, 0x200, v19
	v_lshlrev_b64 v[14:15], 11, v[20:21]
	v_ashrrev_i32_e32 v1, 4, v1
	v_lshl_add_u64 v[14:15], v[4:5], 0, v[14:15]
	v_add_u32_e32 v20, s21, v1
	global_store_dwordx4 v[14:15], v[10:13], off
	v_mad_i64_i32 v[14:15], s[0:1], v20, s96, v[6:7]
	s_nop 1
	v_mad_u64_u32 v[10:11], s[0:1], v1, s3, v[8:9]
	ds_read_b128 v[10:13], v10 offset:36864
	v_ashrrev_i32_e32 v21, 31, v20
	s_waitcnt lgkmcnt(0)
	v_lshlrev_b32_e32 v1, 16, v10
	v_and_b32_e32 v9, 0xffff0000, v10
	s_waitcnt vmcnt(3)
	v_mov_b32_e32 v14, v24
	v_mov_b32_e32 v15, v25
	v_mov_b32_e32 v16, v26
	v_mov_b32_e32 v17, v27
	v_lshlrev_b32_e32 v2, 16, v14
	v_mul_f32_e32 v1, v2, v1
	v_and_b32_e32 v2, 0xffff0000, v14
	v_mul_f32_e32 v2, v2, v9
	v_cvt_pk_bf16_f32 v10, v1, v2
	v_lshlrev_b32_e32 v1, 16, v11
	v_lshlrev_b32_e32 v2, 16, v15
	v_mul_f32_e32 v1, v2, v1
	v_and_b32_e32 v2, 0xffff0000, v15
	v_and_b32_e32 v9, 0xffff0000, v11
	v_mul_f32_e32 v2, v2, v9
	v_cvt_pk_bf16_f32 v11, v1, v2
	v_lshlrev_b32_e32 v1, 16, v12
	v_lshlrev_b32_e32 v2, 16, v16
	v_mul_f32_e32 v1, v2, v1
	v_and_b32_e32 v2, 0xffff0000, v16
	v_and_b32_e32 v9, 0xffff0000, v12
	v_mul_f32_e32 v2, v2, v9
	v_cvt_pk_bf16_f32 v12, v1, v2
	v_lshlrev_b32_e32 v1, 16, v13
	v_lshlrev_b32_e32 v2, 16, v17
	v_mul_f32_e32 v1, v2, v1
	v_and_b32_e32 v2, 0xffff0000, v17
	v_and_b32_e32 v9, 0xffff0000, v13
	v_mul_f32_e32 v2, v2, v9
	v_cvt_pk_bf16_f32 v13, v1, v2
	v_add_u32_e32 v1, 0x400, v19
	v_lshlrev_b64 v[14:15], 11, v[20:21]
	v_ashrrev_i32_e32 v1, 4, v1
	v_lshl_add_u64 v[14:15], v[4:5], 0, v[14:15]
	v_add_u32_e32 v20, s21, v1
	global_store_dwordx4 v[14:15], v[10:13], off
	v_mad_i64_i32 v[14:15], s[0:1], v20, s96, v[6:7]
	s_nop 1
	v_mad_u64_u32 v[10:11], s[0:1], v1, s3, v[8:9]
	ds_read_b128 v[10:13], v10 offset:36864
	v_ashrrev_i32_e32 v21, 31, v20
	s_waitcnt lgkmcnt(0)
	v_lshlrev_b32_e32 v1, 16, v10
	v_and_b32_e32 v9, 0xffff0000, v10
	s_waitcnt vmcnt(3)
	v_mov_b32_e32 v14, v28
	v_mov_b32_e32 v15, v29
	v_mov_b32_e32 v16, v30
	v_mov_b32_e32 v17, v31
	v_lshlrev_b32_e32 v2, 16, v14
	v_mul_f32_e32 v1, v2, v1
	v_and_b32_e32 v2, 0xffff0000, v14
	v_mul_f32_e32 v2, v2, v9
	v_cvt_pk_bf16_f32 v10, v1, v2
	v_lshlrev_b32_e32 v1, 16, v11
	v_lshlrev_b32_e32 v2, 16, v15
	v_mul_f32_e32 v1, v2, v1
	v_and_b32_e32 v2, 0xffff0000, v15
	v_and_b32_e32 v9, 0xffff0000, v11
	v_mul_f32_e32 v2, v2, v9
	v_cvt_pk_bf16_f32 v11, v1, v2
	v_lshlrev_b32_e32 v1, 16, v12
	v_lshlrev_b32_e32 v2, 16, v16
	v_mul_f32_e32 v1, v2, v1
	v_and_b32_e32 v2, 0xffff0000, v16
	v_and_b32_e32 v9, 0xffff0000, v12
	v_mul_f32_e32 v2, v2, v9
	v_cvt_pk_bf16_f32 v12, v1, v2
	v_lshlrev_b32_e32 v1, 16, v13
	v_lshlrev_b32_e32 v2, 16, v17
	v_mul_f32_e32 v1, v2, v1
	v_and_b32_e32 v2, 0xffff0000, v17
	v_and_b32_e32 v9, 0xffff0000, v13
	v_mul_f32_e32 v2, v2, v9
	v_cvt_pk_bf16_f32 v13, v1, v2
	v_add_u32_e32 v1, 0x600, v19
	v_lshlrev_b64 v[14:15], 11, v[20:21]
	v_ashrrev_i32_e32 v1, 4, v1
	v_lshl_add_u64 v[14:15], v[4:5], 0, v[14:15]
	v_mad_u64_u32 v[8:9], s[0:1], v1, s3, v[8:9]
	global_store_dwordx4 v[14:15], v[10:13], off
	ds_read_b128 v[10:13], v8 offset:36864
	v_add_u32_e32 v8, s21, v1
	v_mad_i64_i32 v[6:7], s[0:1], v8, s96, v[6:7]
	s_nop 1
	s_waitcnt lgkmcnt(0)
	v_lshlrev_b32_e32 v1, 16, v10
	v_and_b32_e32 v6, 0xffff0000, v10
	v_ashrrev_i32_e32 v9, 31, v8
	s_waitcnt vmcnt(3)
	v_mov_b32_e32 v14, v32
	v_mov_b32_e32 v15, v33
	v_mov_b32_e32 v16, v34
	v_mov_b32_e32 v17, v35
	v_lshlrev_b32_e32 v2, 16, v14
	v_mul_f32_e32 v1, v2, v1
	v_and_b32_e32 v2, 0xffff0000, v14
	v_mul_f32_e32 v2, v2, v6
	v_cvt_pk_bf16_f32 v10, v1, v2
	v_lshlrev_b32_e32 v1, 16, v11
	v_lshlrev_b32_e32 v2, 16, v15
	v_mul_f32_e32 v1, v2, v1
	v_and_b32_e32 v2, 0xffff0000, v15
	v_and_b32_e32 v6, 0xffff0000, v11
	v_mul_f32_e32 v2, v2, v6
	v_cvt_pk_bf16_f32 v11, v1, v2
	v_lshlrev_b32_e32 v1, 16, v12
	v_lshlrev_b32_e32 v2, 16, v16
	v_mul_f32_e32 v1, v2, v1
	v_and_b32_e32 v2, 0xffff0000, v16
	v_and_b32_e32 v6, 0xffff0000, v12
	v_mul_f32_e32 v2, v2, v6
	v_cvt_pk_bf16_f32 v12, v1, v2
	v_lshlrev_b32_e32 v1, 16, v13
	v_lshlrev_b32_e32 v2, 16, v17
	v_mul_f32_e32 v1, v2, v1
	v_and_b32_e32 v2, 0xffff0000, v17
	v_and_b32_e32 v6, 0xffff0000, v13
	v_mul_f32_e32 v2, v2, v6
	v_lshlrev_b64 v[6:7], 11, v[8:9]
	v_lshl_add_u64 v[4:5], v[4:5], 0, v[6:7]
	v_cvt_pk_bf16_f32 v13, v1, v2
	global_store_dwordx4 v[4:5], v[10:13], off
	s_barrier
	s_cbranch_scc1 .LBB0_1224
